# phase-3 order swap selected by XCD parity (whole XCDs alternate between GLA-local-first and attention-first)
# baseline (speedup 1.0000x reference)
; #define FRESH_TID() do { ap = fresh_args(); ws = ap->ws; unsigned m1_ = ~0u; asm volatile("" : "+s"(m1_)); lane = (int)__builtin_amdgcn_mbcnt_hi(m1_, __builtin_amdgcn_mbcnt_lo(m1_, 0u)); asm volatile("" : "+v"(lane)); wave = wave0; tid = wave0 * 64 + lane; } while (0)
; template <unsigned MASK, bool ONE>
; __global__ void __launch_bounds__(NTHREADS, 2) fwd_kernel(Args a_unused) {
;     ...
;         if (IN(P + 2, 3)) { FRESH_TID();
;             {
;                 const int hw = (vcu >> 5) & 3, dw = tid & 127; float w2[16];
; #pragma unroll
;                 for (int r = 0; r < 16; ++r) w2[r] = (a.w_alpha2 + (size_t)l * 16 * 512)[r * 512 + hw * 128 + dw];
;                 const float bias = (a.b_alpha2 + (size_t)l * 512)[hw * 128 + dw];
;                 for (int u = vcu; u < NB * 4 * 32; u += G) { GlaPre R; gla_local_issue(R, proj, alow, u, tid);
;                     gla_local_unit(lds, R, proj, alow, w2, bias, qdb_, oib_, dstb_, decb_, u, -1, tid, wave, lane); } }
;             FRESH_TID();
;             for (int u = vcu; u < NB * 12 * 16; u += G) { AttnPre R; attn_issue(R, proj, u, tid, wave, lane); attn_unit(lds, R, proj, atto, lse, u, -1, tid, wave, lane); }
.Lsw_start:
	v_readlane_b32 s0, v255, 17
	v_readlane_b32 s1, v255, 18
	s_mov_b32 s1, s97
	v_writelane_b32 v255, s0, 17
	s_mov_b32 s2, s38
	s_waitcnt lgkmcnt(0)
	v_writelane_b32 v255, s1, 18
	v_readlane_b32 s0, v253, 0
	v_readlane_b32 s1, v253, 1
	s_barrier
	s_nop 0
	v_mbcnt_lo_u32_b32 v0, s2, 0
	v_mbcnt_hi_u32_b32 v2, s2, v0
	v_readlane_b32 s2, v253, 10
	v_readlane_b32 s3, v253, 11
	s_andn2_b64 vcc, exec, s[2:3]
	s_cmp_lg_u32 s100, 0
	s_cbranch_scc1 .Lsw_a
	v_readlane_b32 s101, v253, 4
	s_nop 1
	s_bitcmp1_b32 s101, 0
	s_cbranch_scc0 .Lsw_a
	s_mov_b32 s100, 1
	s_branch .LBB0_356
